# bundle3: bundle1 + GLA chunk scan with block-prefetched loads (one wait per 16 steps instead of per step)
# speedup vs baseline: 1.0214x; 1.0103x over previous
.LBB0_523:
	v_ashrrev_i32_e32 v2, 12, v6
	v_and_b32_e32 v0, 0xfc0, v7
	v_ashrrev_i32_e32 v3, 31, v2
	v_and_b32_e32 v4, 0xfff, v7
	v_lshrrev_b32_e32 v5, 4, v0
	v_lshlrev_b64 v[0:1], 21, v[2:3]
	v_lshlrev_b64 v[2:3], 15, v[2:3]
	v_lshl_or_b32 v0, v4, 2, v0
	v_mov_b32_e32 v4, 0
	v_or_b32_e32 v2, v2, v5
	s_movk_i32 s10, 0x80
	v_mov_b32_e32 v5, v4
	s_add_u32 s98, s42, 0xe800000
	s_addc_u32 s99, s43, 0
	s_add_u32 s100, s42, 0x600000
	s_addc_u32 s101, s43, 0
	s_mov_b32 s10, 4
	v_mov_b32_e32 v20, v0
	global_load_dword v36, v20, s[98:99]
	global_load_dword v70, v2, s[100:101]
	v_add_u32_e32 v21, 0x4000, v0
	global_load_dword v37, v21, s[98:99]
	global_load_dword v72, v2, s[100:101] offset:256
	v_add_u32_e32 v22, 0x8000, v0
	global_load_dword v38, v22, s[98:99]
	global_load_dword v74, v2, s[100:101] offset:512
	v_add_u32_e32 v23, 0xc000, v0
	global_load_dword v39, v23, s[98:99]
	global_load_dword v76, v2, s[100:101] offset:768
	v_add_u32_e32 v24, 0x10000, v0
	global_load_dword v40, v24, s[98:99]
	global_load_dword v78, v2, s[100:101] offset:1024
	v_add_u32_e32 v25, 0x14000, v0
	global_load_dword v41, v25, s[98:99]
	global_load_dword v80, v2, s[100:101] offset:1280
	v_add_u32_e32 v26, 0x18000, v0
	global_load_dword v42, v26, s[98:99]
	global_load_dword v82, v2, s[100:101] offset:1536
	v_add_u32_e32 v27, 0x1c000, v0
	global_load_dword v43, v27, s[98:99]
	global_load_dword v84, v2, s[100:101] offset:1792
	v_add_u32_e32 v28, 0x20000, v0
	global_load_dword v44, v28, s[98:99]
	global_load_dword v86, v2, s[100:101] offset:2048
	v_add_u32_e32 v29, 0x24000, v0
	global_load_dword v45, v29, s[98:99]
	global_load_dword v88, v2, s[100:101] offset:2304
	v_add_u32_e32 v30, 0x28000, v0
	global_load_dword v46, v30, s[98:99]
	global_load_dword v90, v2, s[100:101] offset:2560
	v_add_u32_e32 v31, 0x2c000, v0
	global_load_dword v47, v31, s[98:99]
	global_load_dword v92, v2, s[100:101] offset:2816
	v_add_u32_e32 v32, 0x30000, v0
	global_load_dword v48, v32, s[98:99]
	global_load_dword v94, v2, s[100:101] offset:3072
	v_add_u32_e32 v33, 0x34000, v0
	global_load_dword v49, v33, s[98:99]
	global_load_dword v96, v2, s[100:101] offset:3328
	v_add_u32_e32 v34, 0x38000, v0
	global_load_dword v50, v34, s[98:99]
	global_load_dword v98, v2, s[100:101] offset:3584
	v_add_u32_e32 v35, 0x3c000, v0
	global_load_dword v51, v35, s[98:99]
	global_load_dword v100, v2, s[100:101] offset:3840
.Lscan_loop:
	v_add_u32_e32 v0, 0x40000, v0
	v_add_u32_e32 v2, 0x1000, v2
	v_mov_b32_e32 v102, v0
	global_load_dword v118, v102, s[98:99]
	global_load_dword v134, v2, s[100:101]
	v_add_u32_e32 v103, 0x4000, v0
	global_load_dword v119, v103, s[98:99]
	global_load_dword v136, v2, s[100:101] offset:256
	v_add_u32_e32 v104, 0x8000, v0
	global_load_dword v120, v104, s[98:99]
	global_load_dword v138, v2, s[100:101] offset:512
	v_add_u32_e32 v105, 0xc000, v0
	global_load_dword v121, v105, s[98:99]
	global_load_dword v140, v2, s[100:101] offset:768
	v_add_u32_e32 v106, 0x10000, v0
	global_load_dword v122, v106, s[98:99]
	global_load_dword v142, v2, s[100:101] offset:1024
	v_add_u32_e32 v107, 0x14000, v0
	global_load_dword v123, v107, s[98:99]
	global_load_dword v144, v2, s[100:101] offset:1280
	v_add_u32_e32 v108, 0x18000, v0
	global_load_dword v124, v108, s[98:99]
	global_load_dword v146, v2, s[100:101] offset:1536
	v_add_u32_e32 v109, 0x1c000, v0
	global_load_dword v125, v109, s[98:99]
	global_load_dword v148, v2, s[100:101] offset:1792
	v_add_u32_e32 v110, 0x20000, v0
	global_load_dword v126, v110, s[98:99]
	global_load_dword v150, v2, s[100:101] offset:2048
	v_add_u32_e32 v111, 0x24000, v0
	global_load_dword v127, v111, s[98:99]
	global_load_dword v152, v2, s[100:101] offset:2304
	v_add_u32_e32 v112, 0x28000, v0
	global_load_dword v128, v112, s[98:99]
	global_load_dword v154, v2, s[100:101] offset:2560
	v_add_u32_e32 v113, 0x2c000, v0
	global_load_dword v129, v113, s[98:99]
	global_load_dword v156, v2, s[100:101] offset:2816
	v_add_u32_e32 v114, 0x30000, v0
	global_load_dword v130, v114, s[98:99]
	global_load_dword v158, v2, s[100:101] offset:3072
	v_add_u32_e32 v115, 0x34000, v0
	global_load_dword v131, v115, s[98:99]
	global_load_dword v160, v2, s[100:101] offset:3328
	v_add_u32_e32 v116, 0x38000, v0
	global_load_dword v132, v116, s[98:99]
	global_load_dword v162, v2, s[100:101] offset:3584
	v_add_u32_e32 v117, 0x3c000, v0
	global_load_dword v133, v117, s[98:99]
	global_load_dword v164, v2, s[100:101] offset:3840
	s_waitcnt vmcnt(32)
	v_lshlrev_b32_e32 v11, 16, v36
	v_and_b32_e32 v10, 0xffff0000, v36
	v_cvt_pk_bf16_f32 v16, v5, v4
	global_store_dword v20, v16, s[98:99]
	v_pk_fma_f32 v[4:5], v[4:5], v[70:71], v[10:11] op_sel_hi:[1,0,1]
	v_lshlrev_b32_e32 v11, 16, v37
	v_and_b32_e32 v10, 0xffff0000, v37
	v_cvt_pk_bf16_f32 v16, v5, v4
	global_store_dword v21, v16, s[98:99]
	v_pk_fma_f32 v[4:5], v[4:5], v[72:73], v[10:11] op_sel_hi:[1,0,1]
	v_lshlrev_b32_e32 v11, 16, v38
	v_and_b32_e32 v10, 0xffff0000, v38
	v_cvt_pk_bf16_f32 v16, v5, v4
	global_store_dword v22, v16, s[98:99]
	v_pk_fma_f32 v[4:5], v[4:5], v[74:75], v[10:11] op_sel_hi:[1,0,1]
	v_lshlrev_b32_e32 v11, 16, v39
	v_and_b32_e32 v10, 0xffff0000, v39
	v_cvt_pk_bf16_f32 v16, v5, v4
	global_store_dword v23, v16, s[98:99]
	v_pk_fma_f32 v[4:5], v[4:5], v[76:77], v[10:11] op_sel_hi:[1,0,1]
	v_lshlrev_b32_e32 v11, 16, v40
	v_and_b32_e32 v10, 0xffff0000, v40
	v_cvt_pk_bf16_f32 v16, v5, v4
	global_store_dword v24, v16, s[98:99]
	v_pk_fma_f32 v[4:5], v[4:5], v[78:79], v[10:11] op_sel_hi:[1,0,1]
	v_lshlrev_b32_e32 v11, 16, v41
	v_and_b32_e32 v10, 0xffff0000, v41
	v_cvt_pk_bf16_f32 v16, v5, v4
	global_store_dword v25, v16, s[98:99]
	v_pk_fma_f32 v[4:5], v[4:5], v[80:81], v[10:11] op_sel_hi:[1,0,1]
	v_lshlrev_b32_e32 v11, 16, v42
	v_and_b32_e32 v10, 0xffff0000, v42
	v_cvt_pk_bf16_f32 v16, v5, v4
	global_store_dword v26, v16, s[98:99]
	v_pk_fma_f32 v[4:5], v[4:5], v[82:83], v[10:11] op_sel_hi:[1,0,1]
	v_lshlrev_b32_e32 v11, 16, v43
	v_and_b32_e32 v10, 0xffff0000, v43
	v_cvt_pk_bf16_f32 v16, v5, v4
	global_store_dword v27, v16, s[98:99]
	v_pk_fma_f32 v[4:5], v[4:5], v[84:85], v[10:11] op_sel_hi:[1,0,1]
	v_lshlrev_b32_e32 v11, 16, v44
	v_and_b32_e32 v10, 0xffff0000, v44
	v_cvt_pk_bf16_f32 v16, v5, v4
	global_store_dword v28, v16, s[98:99]
	v_pk_fma_f32 v[4:5], v[4:5], v[86:87], v[10:11] op_sel_hi:[1,0,1]
	v_lshlrev_b32_e32 v11, 16, v45
	v_and_b32_e32 v10, 0xffff0000, v45
	v_cvt_pk_bf16_f32 v16, v5, v4
	global_store_dword v29, v16, s[98:99]
	v_pk_fma_f32 v[4:5], v[4:5], v[88:89], v[10:11] op_sel_hi:[1,0,1]
	v_lshlrev_b32_e32 v11, 16, v46
	v_and_b32_e32 v10, 0xffff0000, v46
	v_cvt_pk_bf16_f32 v16, v5, v4
	global_store_dword v30, v16, s[98:99]
	v_pk_fma_f32 v[4:5], v[4:5], v[90:91], v[10:11] op_sel_hi:[1,0,1]
	v_lshlrev_b32_e32 v11, 16, v47
	v_and_b32_e32 v10, 0xffff0000, v47
	v_cvt_pk_bf16_f32 v16, v5, v4
	global_store_dword v31, v16, s[98:99]
	v_pk_fma_f32 v[4:5], v[4:5], v[92:93], v[10:11] op_sel_hi:[1,0,1]
	v_lshlrev_b32_e32 v11, 16, v48
	v_and_b32_e32 v10, 0xffff0000, v48
	v_cvt_pk_bf16_f32 v16, v5, v4
	global_store_dword v32, v16, s[98:99]
	v_pk_fma_f32 v[4:5], v[4:5], v[94:95], v[10:11] op_sel_hi:[1,0,1]
	v_lshlrev_b32_e32 v11, 16, v49
	v_and_b32_e32 v10, 0xffff0000, v49
	v_cvt_pk_bf16_f32 v16, v5, v4
	global_store_dword v33, v16, s[98:99]
	v_pk_fma_f32 v[4:5], v[4:5], v[96:97], v[10:11] op_sel_hi:[1,0,1]
	v_lshlrev_b32_e32 v11, 16, v50
	v_and_b32_e32 v10, 0xffff0000, v50
	v_cvt_pk_bf16_f32 v16, v5, v4
	global_store_dword v34, v16, s[98:99]
	v_pk_fma_f32 v[4:5], v[4:5], v[98:99], v[10:11] op_sel_hi:[1,0,1]
	v_lshlrev_b32_e32 v11, 16, v51
	v_and_b32_e32 v10, 0xffff0000, v51
	v_cvt_pk_bf16_f32 v16, v5, v4
	global_store_dword v35, v16, s[98:99]
	v_pk_fma_f32 v[4:5], v[4:5], v[100:101], v[10:11] op_sel_hi:[1,0,1]
	s_add_i32 s10, s10, -1
	s_cmp_eq_u32 s10, 0
	s_cbranch_scc1 .Lscan_last
	v_add_u32_e32 v0, 0x40000, v0
	v_add_u32_e32 v2, 0x1000, v2
	v_mov_b32_e32 v20, v0
	global_load_dword v36, v20, s[98:99]
	global_load_dword v70, v2, s[100:101]
	v_add_u32_e32 v21, 0x4000, v0
	global_load_dword v37, v21, s[98:99]
	global_load_dword v72, v2, s[100:101] offset:256
	v_add_u32_e32 v22, 0x8000, v0
	global_load_dword v38, v22, s[98:99]
	global_load_dword v74, v2, s[100:101] offset:512
	v_add_u32_e32 v23, 0xc000, v0
	global_load_dword v39, v23, s[98:99]
	global_load_dword v76, v2, s[100:101] offset:768
	v_add_u32_e32 v24, 0x10000, v0
	global_load_dword v40, v24, s[98:99]
	global_load_dword v78, v2, s[100:101] offset:1024
	v_add_u32_e32 v25, 0x14000, v0
	global_load_dword v41, v25, s[98:99]
	global_load_dword v80, v2, s[100:101] offset:1280
	v_add_u32_e32 v26, 0x18000, v0
	global_load_dword v42, v26, s[98:99]
	global_load_dword v82, v2, s[100:101] offset:1536
	v_add_u32_e32 v27, 0x1c000, v0
	global_load_dword v43, v27, s[98:99]
	global_load_dword v84, v2, s[100:101] offset:1792
	v_add_u32_e32 v28, 0x20000, v0
	global_load_dword v44, v28, s[98:99]
	global_load_dword v86, v2, s[100:101] offset:2048
	v_add_u32_e32 v29, 0x24000, v0
	global_load_dword v45, v29, s[98:99]
	global_load_dword v88, v2, s[100:101] offset:2304
	v_add_u32_e32 v30, 0x28000, v0
	global_load_dword v46, v30, s[98:99]
	global_load_dword v90, v2, s[100:101] offset:2560
	v_add_u32_e32 v31, 0x2c000, v0
	global_load_dword v47, v31, s[98:99]
	global_load_dword v92, v2, s[100:101] offset:2816
	v_add_u32_e32 v32, 0x30000, v0
	global_load_dword v48, v32, s[98:99]
	global_load_dword v94, v2, s[100:101] offset:3072
	v_add_u32_e32 v33, 0x34000, v0
	global_load_dword v49, v33, s[98:99]
	global_load_dword v96, v2, s[100:101] offset:3328
	v_add_u32_e32 v34, 0x38000, v0
	global_load_dword v50, v34, s[98:99]
	global_load_dword v98, v2, s[100:101] offset:3584
	v_add_u32_e32 v35, 0x3c000, v0
	global_load_dword v51, v35, s[98:99]
	global_load_dword v100, v2, s[100:101] offset:3840
	s_waitcnt vmcnt(32)
	v_lshlrev_b32_e32 v11, 16, v118
	v_and_b32_e32 v10, 0xffff0000, v118
	v_cvt_pk_bf16_f32 v16, v5, v4
	global_store_dword v102, v16, s[98:99]
	v_pk_fma_f32 v[4:5], v[4:5], v[134:135], v[10:11] op_sel_hi:[1,0,1]
	v_lshlrev_b32_e32 v11, 16, v119
	v_and_b32_e32 v10, 0xffff0000, v119
	v_cvt_pk_bf16_f32 v16, v5, v4
	global_store_dword v103, v16, s[98:99]
	v_pk_fma_f32 v[4:5], v[4:5], v[136:137], v[10:11] op_sel_hi:[1,0,1]
	v_lshlrev_b32_e32 v11, 16, v120
	v_and_b32_e32 v10, 0xffff0000, v120
	v_cvt_pk_bf16_f32 v16, v5, v4
	global_store_dword v104, v16, s[98:99]
	v_pk_fma_f32 v[4:5], v[4:5], v[138:139], v[10:11] op_sel_hi:[1,0,1]
	v_lshlrev_b32_e32 v11, 16, v121
	v_and_b32_e32 v10, 0xffff0000, v121
	v_cvt_pk_bf16_f32 v16, v5, v4
	global_store_dword v105, v16, s[98:99]
	v_pk_fma_f32 v[4:5], v[4:5], v[140:141], v[10:11] op_sel_hi:[1,0,1]
	v_lshlrev_b32_e32 v11, 16, v122
	v_and_b32_e32 v10, 0xffff0000, v122
	v_cvt_pk_bf16_f32 v16, v5, v4
	global_store_dword v106, v16, s[98:99]
	v_pk_fma_f32 v[4:5], v[4:5], v[142:143], v[10:11] op_sel_hi:[1,0,1]
	v_lshlrev_b32_e32 v11, 16, v123
	v_and_b32_e32 v10, 0xffff0000, v123
	v_cvt_pk_bf16_f32 v16, v5, v4
	global_store_dword v107, v16, s[98:99]
	v_pk_fma_f32 v[4:5], v[4:5], v[144:145], v[10:11] op_sel_hi:[1,0,1]
	v_lshlrev_b32_e32 v11, 16, v124
	v_and_b32_e32 v10, 0xffff0000, v124
	v_cvt_pk_bf16_f32 v16, v5, v4
	global_store_dword v108, v16, s[98:99]
	v_pk_fma_f32 v[4:5], v[4:5], v[146:147], v[10:11] op_sel_hi:[1,0,1]
	v_lshlrev_b32_e32 v11, 16, v125
	v_and_b32_e32 v10, 0xffff0000, v125
	v_cvt_pk_bf16_f32 v16, v5, v4
	global_store_dword v109, v16, s[98:99]
	v_pk_fma_f32 v[4:5], v[4:5], v[148:149], v[10:11] op_sel_hi:[1,0,1]
	v_lshlrev_b32_e32 v11, 16, v126
	v_and_b32_e32 v10, 0xffff0000, v126
	v_cvt_pk_bf16_f32 v16, v5, v4
	global_store_dword v110, v16, s[98:99]
	v_pk_fma_f32 v[4:5], v[4:5], v[150:151], v[10:11] op_sel_hi:[1,0,1]
	v_lshlrev_b32_e32 v11, 16, v127
	v_and_b32_e32 v10, 0xffff0000, v127
	v_cvt_pk_bf16_f32 v16, v5, v4
	global_store_dword v111, v16, s[98:99]
	v_pk_fma_f32 v[4:5], v[4:5], v[152:153], v[10:11] op_sel_hi:[1,0,1]
	v_lshlrev_b32_e32 v11, 16, v128
	v_and_b32_e32 v10, 0xffff0000, v128
	v_cvt_pk_bf16_f32 v16, v5, v4
	global_store_dword v112, v16, s[98:99]
	v_pk_fma_f32 v[4:5], v[4:5], v[154:155], v[10:11] op_sel_hi:[1,0,1]
	v_lshlrev_b32_e32 v11, 16, v129
	v_and_b32_e32 v10, 0xffff0000, v129
	v_cvt_pk_bf16_f32 v16, v5, v4
	global_store_dword v113, v16, s[98:99]
	v_pk_fma_f32 v[4:5], v[4:5], v[156:157], v[10:11] op_sel_hi:[1,0,1]
	v_lshlrev_b32_e32 v11, 16, v130
	v_and_b32_e32 v10, 0xffff0000, v130
	v_cvt_pk_bf16_f32 v16, v5, v4
	global_store_dword v114, v16, s[98:99]
	v_pk_fma_f32 v[4:5], v[4:5], v[158:159], v[10:11] op_sel_hi:[1,0,1]
	v_lshlrev_b32_e32 v11, 16, v131
	v_and_b32_e32 v10, 0xffff0000, v131
	v_cvt_pk_bf16_f32 v16, v5, v4
	global_store_dword v115, v16, s[98:99]
	v_pk_fma_f32 v[4:5], v[4:5], v[160:161], v[10:11] op_sel_hi:[1,0,1]
	v_lshlrev_b32_e32 v11, 16, v132
	v_and_b32_e32 v10, 0xffff0000, v132
	v_cvt_pk_bf16_f32 v16, v5, v4
	global_store_dword v116, v16, s[98:99]
	v_pk_fma_f32 v[4:5], v[4:5], v[162:163], v[10:11] op_sel_hi:[1,0,1]
	v_lshlrev_b32_e32 v11, 16, v133
	v_and_b32_e32 v10, 0xffff0000, v133
	v_cvt_pk_bf16_f32 v16, v5, v4
	global_store_dword v117, v16, s[98:99]
	v_pk_fma_f32 v[4:5], v[4:5], v[164:165], v[10:11] op_sel_hi:[1,0,1]
	s_branch .Lscan_loop
.Lscan_last:
	s_waitcnt vmcnt(0)
	v_lshlrev_b32_e32 v11, 16, v118
	v_and_b32_e32 v10, 0xffff0000, v118
	v_cvt_pk_bf16_f32 v16, v5, v4
	global_store_dword v102, v16, s[98:99]
	v_pk_fma_f32 v[4:5], v[4:5], v[134:135], v[10:11] op_sel_hi:[1,0,1]
	v_lshlrev_b32_e32 v11, 16, v119
	v_and_b32_e32 v10, 0xffff0000, v119
	v_cvt_pk_bf16_f32 v16, v5, v4
	global_store_dword v103, v16, s[98:99]
	v_pk_fma_f32 v[4:5], v[4:5], v[136:137], v[10:11] op_sel_hi:[1,0,1]
	v_lshlrev_b32_e32 v11, 16, v120
	v_and_b32_e32 v10, 0xffff0000, v120
	v_cvt_pk_bf16_f32 v16, v5, v4
	global_store_dword v104, v16, s[98:99]
	v_pk_fma_f32 v[4:5], v[4:5], v[138:139], v[10:11] op_sel_hi:[1,0,1]
	v_lshlrev_b32_e32 v11, 16, v121
	v_and_b32_e32 v10, 0xffff0000, v121
	v_cvt_pk_bf16_f32 v16, v5, v4
	global_store_dword v105, v16, s[98:99]
	v_pk_fma_f32 v[4:5], v[4:5], v[140:141], v[10:11] op_sel_hi:[1,0,1]
	v_lshlrev_b32_e32 v11, 16, v122
	v_and_b32_e32 v10, 0xffff0000, v122
	v_cvt_pk_bf16_f32 v16, v5, v4
	global_store_dword v106, v16, s[98:99]
	v_pk_fma_f32 v[4:5], v[4:5], v[142:143], v[10:11] op_sel_hi:[1,0,1]
	v_lshlrev_b32_e32 v11, 16, v123
	v_and_b32_e32 v10, 0xffff0000, v123
	v_cvt_pk_bf16_f32 v16, v5, v4
	global_store_dword v107, v16, s[98:99]
	v_pk_fma_f32 v[4:5], v[4:5], v[144:145], v[10:11] op_sel_hi:[1,0,1]
	v_lshlrev_b32_e32 v11, 16, v124
	v_and_b32_e32 v10, 0xffff0000, v124
	v_cvt_pk_bf16_f32 v16, v5, v4
	global_store_dword v108, v16, s[98:99]
	v_pk_fma_f32 v[4:5], v[4:5], v[146:147], v[10:11] op_sel_hi:[1,0,1]
	v_lshlrev_b32_e32 v11, 16, v125
	v_and_b32_e32 v10, 0xffff0000, v125
	v_cvt_pk_bf16_f32 v16, v5, v4
	global_store_dword v109, v16, s[98:99]
	v_pk_fma_f32 v[4:5], v[4:5], v[148:149], v[10:11] op_sel_hi:[1,0,1]
	v_lshlrev_b32_e32 v11, 16, v126
	v_and_b32_e32 v10, 0xffff0000, v126
	v_cvt_pk_bf16_f32 v16, v5, v4
	global_store_dword v110, v16, s[98:99]
	v_pk_fma_f32 v[4:5], v[4:5], v[150:151], v[10:11] op_sel_hi:[1,0,1]
	v_lshlrev_b32_e32 v11, 16, v127
	v_and_b32_e32 v10, 0xffff0000, v127
	v_cvt_pk_bf16_f32 v16, v5, v4
	global_store_dword v111, v16, s[98:99]
	v_pk_fma_f32 v[4:5], v[4:5], v[152:153], v[10:11] op_sel_hi:[1,0,1]
	v_lshlrev_b32_e32 v11, 16, v128
	v_and_b32_e32 v10, 0xffff0000, v128
	v_cvt_pk_bf16_f32 v16, v5, v4
	global_store_dword v112, v16, s[98:99]
	v_pk_fma_f32 v[4:5], v[4:5], v[154:155], v[10:11] op_sel_hi:[1,0,1]
	v_lshlrev_b32_e32 v11, 16, v129
	v_and_b32_e32 v10, 0xffff0000, v129
	v_cvt_pk_bf16_f32 v16, v5, v4
	global_store_dword v113, v16, s[98:99]
	v_pk_fma_f32 v[4:5], v[4:5], v[156:157], v[10:11] op_sel_hi:[1,0,1]
	v_lshlrev_b32_e32 v11, 16, v130
	v_and_b32_e32 v10, 0xffff0000, v130
	v_cvt_pk_bf16_f32 v16, v5, v4
	global_store_dword v114, v16, s[98:99]
	v_pk_fma_f32 v[4:5], v[4:5], v[158:159], v[10:11] op_sel_hi:[1,0,1]
	v_lshlrev_b32_e32 v11, 16, v131
	v_and_b32_e32 v10, 0xffff0000, v131
	v_cvt_pk_bf16_f32 v16, v5, v4
	global_store_dword v115, v16, s[98:99]
	v_pk_fma_f32 v[4:5], v[4:5], v[160:161], v[10:11] op_sel_hi:[1,0,1]
	v_lshlrev_b32_e32 v11, 16, v132
	v_and_b32_e32 v10, 0xffff0000, v132
	v_cvt_pk_bf16_f32 v16, v5, v4
	global_store_dword v116, v16, s[98:99]
	v_pk_fma_f32 v[4:5], v[4:5], v[162:163], v[10:11] op_sel_hi:[1,0,1]
	v_lshlrev_b32_e32 v11, 16, v133
	v_and_b32_e32 v10, 0xffff0000, v133
	v_cvt_pk_bf16_f32 v16, v5, v4
	global_store_dword v117, v16, s[98:99]
	v_pk_fma_f32 v[4:5], v[4:5], v[164:165], v[10:11] op_sel_hi:[1,0,1]
	v_add_u32_e32 v6, s62, v6
	s_mov_b32 s10, 0x1ffff
	v_cmp_lt_i32_e32 vcc, s10, v6
	s_or_b64 s[8:9], vcc, s[8:9]
	v_add_u16_e32 v7, s62, v7
	s_andn2_b64 exec, exec, s[8:9]
	s_cbranch_execnz .LBB0_523

	.amdhsa_kernel _Z6mk_fwd4Args
		.amdhsa_group_segment_fixed_size 0
		.amdhsa_private_segment_fixed_size 0
		.amdhsa_kernarg_size 488
		.amdhsa_user_sgpr_count 2
		.amdhsa_user_sgpr_dispatch_ptr 0
		.amdhsa_user_sgpr_queue_ptr 0
		.amdhsa_user_sgpr_kernarg_segment_ptr 1
		.amdhsa_user_sgpr_dispatch_id 0
		.amdhsa_user_sgpr_kernarg_preload_length 0
		.amdhsa_user_sgpr_kernarg_preload_offset 0
		.amdhsa_user_sgpr_private_segment_size 0
		.amdhsa_uses_dynamic_stack 0
		.amdhsa_enable_private_segment 0
		.amdhsa_system_sgpr_workgroup_id_x 1
		.amdhsa_system_sgpr_workgroup_id_y 0
		.amdhsa_system_sgpr_workgroup_id_z 0
		.amdhsa_system_sgpr_workgroup_info 0
		.amdhsa_system_vgpr_workitem_id 0
		.amdhsa_next_free_vgpr 256
		.amdhsa_next_free_sgpr 102
		.amdhsa_accum_offset 256
		.amdhsa_reserve_vcc 1
		.amdhsa_float_round_mode_32 0
		.amdhsa_float_round_mode_16_64 0
		.amdhsa_float_denorm_mode_32 3
		.amdhsa_float_denorm_mode_16_64 3
		.amdhsa_dx10_clamp 1
		.amdhsa_ieee_mode 1
		.amdhsa_fp16_overflow 0
		.amdhsa_tg_split 0
		.amdhsa_exception_fp_ieee_invalid_op 0
		.amdhsa_exception_fp_denorm_src 0
		.amdhsa_exception_fp_ieee_div_zero 0
		.amdhsa_exception_fp_ieee_overflow 0
		.amdhsa_exception_fp_ieee_underflow 0
		.amdhsa_exception_fp_ieee_inexact 0
		.amdhsa_exception_int_div_zero 0
	.end_amdhsa_kernel

amdhsa.kernels:
  - .agpr_count:     0
    .args:
      - .offset:         0
        .size:           232
        .value_kind:     by_value
      - .offset:         232
        .size:           4
        .value_kind:     hidden_block_count_x
      - .offset:         236
        .size:           4
        .value_kind:     hidden_block_count_y
      - .offset:         240
        .size:           4
        .value_kind:     hidden_block_count_z
      - .offset:         244
        .size:           2
        .value_kind:     hidden_group_size_x
      - .offset:         246
        .size:           2
        .value_kind:     hidden_group_size_y
      - .offset:         248
        .size:           2
        .value_kind:     hidden_group_size_z
      - .offset:         250
        .size:           2
        .value_kind:     hidden_remainder_x
      - .offset:         252
        .size:           2
        .value_kind:     hidden_remainder_y
      - .offset:         254
        .size:           2
        .value_kind:     hidden_remainder_z
      - .offset:         272
        .size:           8
        .value_kind:     hidden_global_offset_x
      - .offset:         280
        .size:           8
        .value_kind:     hidden_global_offset_y
      - .offset:         288
        .size:           8
        .value_kind:     hidden_global_offset_z
      - .offset:         296
        .size:           2
        .value_kind:     hidden_grid_dims
      - .offset:         352
        .size:           4
        .value_kind:     hidden_dynamic_lds_size
    .group_segment_fixed_size: 0
    .kernarg_segment_align: 8
    .kernarg_segment_size: 488
    .language:       OpenCL C
    .language_version:
      - 2
      - 0
    .max_flat_workgroup_size: 512
    .name:           _Z6mk_fwd4Args
    .private_segment_fixed_size: 0
    .sgpr_count:     108
    .sgpr_spill_count: 113
    .symbol:         _Z6mk_fwd4Args.kd
    .uniform_work_group_size: 1
    .uses_dynamic_stack: false
    .vgpr_count:     256
    .vgpr_spill_count: 0
    .wavefront_size: 64
